# baseline (speedup 1.0000x reference)
.LBB2_3:
	s_mul_i32 s15, s14, 0xe000
	s_add_i32 s14, s14, 1
	s_cmp_lg_u32 s14, 2
	s_cselect_b32 s14, s14, 0
	s_add_i32 s20, s15, s21
	v_add3_u32 v206, s15, v147, v148
	v_add3_u32 v207, s15, v146, v148
	s_waitcnt lgkmcnt(8)
	v_mfma_f32_16x16x32_f16 v[134:137], v[98:101], v[118:121], v[134:137]
	s_waitcnt lgkmcnt(7)
	v_mfma_f32_16x16x32_f16 v[130:133], v[90:93], v[118:121], v[130:133]
	s_waitcnt lgkmcnt(6)
	v_mfma_f32_16x16x32_f16 v[102:105], v[98:101], v[106:109], v[102:105]
	ds_read_b128 v[152:155], v206
	v_mfma_f32_16x16x32_f16 v[94:97], v[90:93], v[106:109], v[94:97]
	ds_read_b128 v[168:171], v207 offset:32768
	s_waitcnt lgkmcnt(7)
	v_mfma_f32_16x16x32_f16 v[126:129], v[82:85], v[118:121], v[126:129]
	ds_read_b128 v[172:175], v207 offset:34816
	v_mfma_f32_16x16x32_f16 v[78:81], v[82:85], v[106:109], v[78:81]
	ds_read_b128 v[156:159], v206 offset:2048
	s_waitcnt lgkmcnt(8)
	v_mfma_f32_16x16x32_f16 v[122:125], v[74:77], v[118:121], v[122:125]
	ds_read_b128 v[176:179], v207 offset:36864
	v_mfma_f32_16x16x32_f16 v[70:73], v[74:77], v[106:109], v[70:73]
	ds_read_b128 v[180:183], v207 offset:38912
	s_waitcnt lgkmcnt(9)
	v_mfma_f32_16x16x32_f16 v[54:57], v[98:101], v[86:89], v[54:57]
	ds_read_b128 v[160:163], v206 offset:4096
	v_mfma_f32_16x16x32_f16 v[46:49], v[90:93], v[86:89], v[46:49]
	ds_read_b128 v[184:187], v207 offset:40960
	v_mfma_f32_16x16x32_f16 v[42:45], v[82:85], v[86:89], v[42:45]
	ds_read_b128 v[188:191], v207 offset:43008
	v_mfma_f32_16x16x32_f16 v[38:41], v[74:77], v[86:89], v[38:41]
	ds_read_b128 v[164:167], v206 offset:6144
	s_waitcnt lgkmcnt(12)
	v_mfma_f32_16x16x32_f16 v[114:117], v[66:69], v[118:121], v[114:117]
	v_mfma_f32_16x16x32_f16 v[62:65], v[66:69], v[106:109], v[62:65]
	v_mfma_f32_16x16x32_f16 v[30:33], v[66:69], v[86:89], v[30:33]
	s_waitcnt lgkmcnt(11)
	v_mfma_f32_16x16x32_f16 v[110:113], v[50:53], v[118:121], v[110:113]
	v_mfma_f32_16x16x32_f16 v[58:61], v[50:53], v[106:109], v[58:61]
	v_mfma_f32_16x16x32_f16 v[26:29], v[50:53], v[86:89], v[26:29]
	s_waitcnt lgkmcnt(10)
	v_mfma_f32_16x16x32_f16 v[22:25], v[98:101], v[34:37], v[22:25]
	v_mfma_f32_16x16x32_f16 v[18:21], v[90:93], v[34:37], v[18:21]
	v_mfma_f32_16x16x32_f16 v[14:17], v[82:85], v[34:37], v[14:17]
	v_mfma_f32_16x16x32_f16 v[10:13], v[74:77], v[34:37], v[10:13]
	v_mfma_f32_16x16x32_f16 v[6:9], v[66:69], v[34:37], v[6:9]
	v_mfma_f32_16x16x32_f16 v[2:5], v[50:53], v[34:37], v[2:5]
	s_waitcnt vmcnt(0) lgkmcnt(0)
	s_barrier
	s_mov_b32 m0, s20
	s_mul_i32 s15, s14, 0xe000
	v_mfma_f32_16x16x32_f16 v[134:137], v[168:171], v[152:155], v[134:137]
	global_load_lds_dwordx4 v[192:193], off
	v_lshl_add_u64 v[192:193], v[192:193], 0, s[22:23]
	s_add_u32 m0, s20, 0x2000
	v_mfma_f32_16x16x32_f16 v[130:133], v[172:175], v[152:155], v[130:133]
	v_mfma_f32_16x16x32_f16 v[126:129], v[176:179], v[152:155], v[126:129]
	global_load_lds_dwordx4 v[194:195], off
	v_lshl_add_u64 v[194:195], v[194:195], 0, s[22:23]
	s_add_u32 m0, s20, 0x4000
	v_mfma_f32_16x16x32_f16 v[122:125], v[180:183], v[152:155], v[122:125]
	v_mfma_f32_16x16x32_f16 v[114:117], v[184:187], v[152:155], v[114:117]
	global_load_lds_dwordx4 v[196:197], off
	v_lshl_add_u64 v[196:197], v[196:197], 0, s[22:23]
	s_add_u32 m0, s20, 0x6000
	v_mfma_f32_16x16x32_f16 v[110:113], v[188:191], v[152:155], v[110:113]
	v_mfma_f32_16x16x32_f16 v[102:105], v[168:171], v[156:159], v[102:105]
	global_load_lds_dwordx4 v[198:199], off
	v_lshl_add_u64 v[198:199], v[198:199], 0, s[22:23]
	s_add_u32 m0, s20, 0x8000
	v_mfma_f32_16x16x32_f16 v[94:97], v[172:175], v[156:159], v[94:97]
	v_mfma_f32_16x16x32_f16 v[78:81], v[176:179], v[156:159], v[78:81]
	global_load_lds_dwordx4 v[200:201], off
	v_lshl_add_u64 v[200:201], v[200:201], 0, s[22:23]
	s_add_u32 m0, s20, 0xa000
	v_mfma_f32_16x16x32_f16 v[70:73], v[180:183], v[156:159], v[70:73]
	v_mfma_f32_16x16x32_f16 v[62:65], v[184:187], v[156:159], v[62:65]
	global_load_lds_dwordx4 v[202:203], off
	v_lshl_add_u64 v[202:203], v[202:203], 0, s[22:23]
	s_add_u32 m0, s20, 0xc000
	v_mfma_f32_16x16x32_f16 v[58:61], v[188:191], v[156:159], v[58:61]
	v_mfma_f32_16x16x32_f16 v[54:57], v[168:171], v[160:163], v[54:57]
	global_load_lds_dwordx4 v[204:205], off
	v_lshl_add_u64 v[204:205], v[204:205], 0, s[22:23]
	v_add_u32_e32 v206, s15, v150
	v_add_u32_e32 v207, s15, v151
	v_mfma_f32_16x16x32_f16 v[46:49], v[172:175], v[160:163], v[46:49]
	v_mfma_f32_16x16x32_f16 v[42:45], v[176:179], v[160:163], v[42:45]
	ds_read_b128 v[118:121], v206
	v_mfma_f32_16x16x32_f16 v[38:41], v[180:183], v[160:163], v[38:41]
	ds_read_b128 v[98:101], v207 offset:32768
	v_mfma_f32_16x16x32_f16 v[30:33], v[184:187], v[160:163], v[30:33]
	ds_read_b128 v[90:93], v207 offset:34816
	v_mfma_f32_16x16x32_f16 v[26:29], v[188:191], v[160:163], v[26:29]
	ds_read_b128 v[106:109], v206 offset:2048
	v_mfma_f32_16x16x32_f16 v[22:25], v[168:171], v[164:167], v[22:25]
	ds_read_b128 v[82:85], v207 offset:36864
	v_mfma_f32_16x16x32_f16 v[18:21], v[172:175], v[164:167], v[18:21]
	ds_read_b128 v[74:77], v207 offset:38912
	v_mfma_f32_16x16x32_f16 v[14:17], v[176:179], v[164:167], v[14:17]
	ds_read_b128 v[86:89], v206 offset:4096
	v_mfma_f32_16x16x32_f16 v[10:13], v[180:183], v[164:167], v[10:13]
	ds_read_b128 v[66:69], v207 offset:40960
	v_mfma_f32_16x16x32_f16 v[6:9], v[184:187], v[164:167], v[6:9]
	ds_read_b128 v[50:53], v207 offset:43008
	v_mfma_f32_16x16x32_f16 v[2:5], v[188:191], v[164:167], v[2:5]
	ds_read_b128 v[34:37], v206 offset:6144
	s_add_u32 s0, s0, 0x80
	s_addc_u32 s1, s1, 0
	s_cmpk_eq_i32 s0, 0x700
	s_cbranch_scc0 .LBB2_3
	s_add_i32 s0, s15, 0
	v_add3_u32 v0, s0, v147, v148
	s_waitcnt lgkmcnt(0)
	v_mfma_f32_16x16x32_f16 v[134:137], v[98:101], v[118:121], v[134:137]
	s_add_i32 s1, s14, 1
	s_cmp_lg_u32 s1, 2
	s_cselect_b32 s1, s1, 0
	v_mfma_f32_16x16x32_f16 v[130:133], v[90:93], v[118:121], v[130:133]
	v_mfma_f32_16x16x32_f16 v[126:129], v[82:85], v[118:121], v[126:129]
	v_mfma_f32_16x16x32_f16 v[102:105], v[98:101], v[106:109], v[102:105]
	v_mfma_f32_16x16x32_f16 v[94:97], v[90:93], v[106:109], v[94:97]
	v_mfma_f32_16x16x32_f16 v[78:81], v[82:85], v[106:109], v[78:81]
	v_mfma_f32_16x16x32_f16 v[54:57], v[98:101], v[86:89], v[54:57]
	v_mfma_f32_16x16x32_f16 v[46:49], v[90:93], v[86:89], v[46:49]
	v_mfma_f32_16x16x32_f16 v[42:45], v[82:85], v[86:89], v[42:45]
	v_mfma_f32_16x16x32_f16 v[38:41], v[74:77], v[86:89], v[38:41]
	v_mfma_f32_16x16x32_f16 v[30:33], v[66:69], v[86:89], v[30:33]
	v_mfma_f32_16x16x32_f16 v[26:29], v[50:53], v[86:89], v[26:29]
	v_mfma_f32_16x16x32_f16 v[22:25], v[98:101], v[34:37], v[22:25]
	v_mfma_f32_16x16x32_f16 v[18:21], v[90:93], v[34:37], v[18:21]
	ds_read_b128 v[86:89], v0
	ds_read_b128 v[90:93], v0 offset:2048
	v_mfma_f32_16x16x32_f16 v[14:17], v[82:85], v[34:37], v[14:17]
	ds_read_b128 v[82:85], v0 offset:4096
	ds_read_b128 v[98:101], v0 offset:6144
	v_add3_u32 v0, s0, v146, v148
	v_mfma_f32_16x16x32_f16 v[122:125], v[74:77], v[118:121], v[122:125]
	v_mfma_f32_16x16x32_f16 v[114:117], v[66:69], v[118:121], v[114:117]
	v_mfma_f32_16x16x32_f16 v[110:113], v[50:53], v[118:121], v[110:113]
	v_mfma_f32_16x16x32_f16 v[70:73], v[74:77], v[106:109], v[70:73]
	v_mfma_f32_16x16x32_f16 v[62:65], v[66:69], v[106:109], v[62:65]
	v_mfma_f32_16x16x32_f16 v[58:61], v[50:53], v[106:109], v[58:61]
	v_mfma_f32_16x16x32_f16 v[10:13], v[74:77], v[34:37], v[10:13]
	ds_read_b128 v[74:77], v0 offset:32768
	ds_read_b128 v[106:109], v0 offset:34816
	v_mfma_f32_16x16x32_f16 v[6:9], v[66:69], v[34:37], v[6:9]
	ds_read_b128 v[66:69], v0 offset:36864
	ds_read_b128 v[118:121], v0 offset:38912
	ds_read_b128 v[152:155], v0 offset:40960
	ds_read_b128 v[156:159], v0 offset:43008
	v_mfma_f32_16x16x32_f16 v[0:3], v[50:53], v[34:37], v[2:5]
	s_mul_i32 s1, s1, 0xe000
	s_waitcnt vmcnt(0) lgkmcnt(0)
	s_barrier
	v_add_u32_e32 v4, s1, v150
	ds_read_b128 v[34:37], v4
	ds_read_b128 v[50:53], v4 offset:2048
	ds_read_b128 v[160:163], v4 offset:4096
	ds_read_b128 v[164:167], v4 offset:6144
	v_add_u32_e32 v4, s1, v151
	ds_read_b128 v[168:171], v4 offset:32768
	ds_read_b128 v[172:175], v4 offset:34816
	ds_read_b128 v[176:179], v4 offset:36864
	ds_read_b128 v[180:183], v4 offset:38912
	ds_read_b128 v[184:187], v4 offset:40960
	ds_read_b128 v[188:191], v4 offset:43008
	v_mfma_f32_16x16x32_f16 v[134:137], v[74:77], v[86:89], v[134:137]
	v_mfma_f32_16x16x32_f16 v[130:133], v[106:109], v[86:89], v[130:133]
	v_mfma_f32_16x16x32_f16 v[126:129], v[66:69], v[86:89], v[126:129]
	v_mfma_f32_16x16x32_f16 v[122:125], v[118:121], v[86:89], v[122:125]
	v_mfma_f32_16x16x32_f16 v[114:117], v[152:155], v[86:89], v[114:117]
	v_mfma_f32_16x16x32_f16 v[86:89], v[156:159], v[86:89], v[110:113]
	v_mfma_f32_16x16x32_f16 v[102:105], v[74:77], v[90:93], v[102:105]
	v_mfma_f32_16x16x32_f16 v[94:97], v[106:109], v[90:93], v[94:97]
	v_mfma_f32_16x16x32_f16 v[78:81], v[66:69], v[90:93], v[78:81]
	v_mfma_f32_16x16x32_f16 v[70:73], v[118:121], v[90:93], v[70:73]
	v_mfma_f32_16x16x32_f16 v[62:65], v[152:155], v[90:93], v[62:65]
	v_mfma_f32_16x16x32_f16 v[58:61], v[156:159], v[90:93], v[58:61]
	v_mfma_f32_16x16x32_f16 v[54:57], v[74:77], v[82:85], v[54:57]
	v_mfma_f32_16x16x32_f16 v[46:49], v[106:109], v[82:85], v[46:49]
	v_mfma_f32_16x16x32_f16 v[42:45], v[66:69], v[82:85], v[42:45]
	v_mfma_f32_16x16x32_f16 v[38:41], v[118:121], v[82:85], v[38:41]
	v_mfma_f32_16x16x32_f16 v[30:33], v[152:155], v[82:85], v[30:33]
	v_mfma_f32_16x16x32_f16 v[26:29], v[156:159], v[82:85], v[26:29]
	v_mfma_f32_16x16x32_f16 v[22:25], v[74:77], v[98:101], v[22:25]
	v_mfma_f32_16x16x32_f16 v[18:21], v[106:109], v[98:101], v[18:21]
	v_mfma_f32_16x16x32_f16 v[14:17], v[66:69], v[98:101], v[14:17]
	v_mfma_f32_16x16x32_f16 v[10:13], v[118:121], v[98:101], v[10:13]
	v_mfma_f32_16x16x32_f16 v[4:7], v[152:155], v[98:101], v[6:9]
	v_mfma_f32_16x16x32_f16 v[0:3], v[156:159], v[98:101], v[0:3]
	s_add_i32 s0, s1, 0
	s_nop 0
	v_add3_u32 v8, s0, v147, v148
	s_waitcnt lgkmcnt(5)
	v_mfma_f32_16x16x32_f16 v[66:69], v[168:171], v[34:37], v[134:137]
	s_waitcnt lgkmcnt(4)
	v_mfma_f32_16x16x32_f16 v[74:77], v[172:175], v[34:37], v[130:133]
	s_waitcnt lgkmcnt(3)
	v_mfma_f32_16x16x32_f16 v[82:85], v[176:179], v[34:37], v[126:129]
	s_waitcnt lgkmcnt(2)
	v_mfma_f32_16x16x32_f16 v[90:93], v[180:183], v[34:37], v[122:125]
	s_waitcnt lgkmcnt(1)
	v_mfma_f32_16x16x32_f16 v[98:101], v[184:187], v[34:37], v[114:117]
	s_waitcnt lgkmcnt(0)
	v_mfma_f32_16x16x32_f16 v[34:37], v[188:191], v[34:37], v[86:89]
	v_mfma_f32_16x16x32_f16 v[86:89], v[168:171], v[50:53], v[102:105]
	v_mfma_f32_16x16x32_f16 v[94:97], v[172:175], v[50:53], v[94:97]
	v_mfma_f32_16x16x32_f16 v[78:81], v[176:179], v[50:53], v[78:81]
	v_mfma_f32_16x16x32_f16 v[70:73], v[180:183], v[50:53], v[70:73]
	v_mfma_f32_16x16x32_f16 v[62:65], v[184:187], v[50:53], v[62:65]
	v_mfma_f32_16x16x32_f16 v[50:53], v[188:191], v[50:53], v[58:61]
	s_nop 2
	ds_read_b128 v[58:61], v8
	ds_read_b128 v[102:105], v8 offset:2048
	ds_read_b128 v[106:109], v8 offset:4096
	ds_read_b128 v[110:113], v8 offset:6144
	v_mfma_f32_16x16x32_f16 v[8:11], v[180:183], v[164:167], v[10:13]
	s_nop 2
	v_add3_u32 v12, s0, v146, v148
	ds_read_b128 v[114:117], v12 offset:32768
	ds_read_b128 v[118:121], v12 offset:34816
	ds_read_b128 v[122:125], v12 offset:36864
	ds_read_b128 v[126:129], v12 offset:38912
	ds_read_b128 v[130:133], v12 offset:40960
	ds_read_b128 v[134:137], v12 offset:43008
	v_mfma_f32_16x16x32_f16 v[54:57], v[168:171], v[160:163], v[54:57]
	v_mfma_f32_16x16x32_f16 v[46:49], v[172:175], v[160:163], v[46:49]
	v_mfma_f32_16x16x32_f16 v[42:45], v[176:179], v[160:163], v[42:45]
	v_mfma_f32_16x16x32_f16 v[38:41], v[180:183], v[160:163], v[38:41]
	v_mfma_f32_16x16x32_f16 v[30:33], v[184:187], v[160:163], v[30:33]
	v_mfma_f32_16x16x32_f16 v[26:29], v[188:191], v[160:163], v[26:29]
	v_mfma_f32_16x16x32_f16 v[22:25], v[168:171], v[164:167], v[22:25]
	v_mfma_f32_16x16x32_f16 v[18:21], v[172:175], v[164:167], v[18:21]
	v_mfma_f32_16x16x32_f16 v[14:17], v[176:179], v[164:167], v[14:17]
	v_mfma_f32_16x16x32_f16 v[4:7], v[184:187], v[164:167], v[4:7]
	v_mfma_f32_16x16x32_f16 v[0:3], v[188:191], v[164:167], v[0:3]
	s_waitcnt vmcnt(0) lgkmcnt(0)
	s_barrier
	v_mfma_f32_16x16x32_f16 v[66:69], v[114:117], v[58:61], v[66:69]
	v_mfma_f32_16x16x32_f16 v[74:77], v[118:121], v[58:61], v[74:77]
	v_mfma_f32_16x16x32_f16 v[82:85], v[122:125], v[58:61], v[82:85]
	v_mfma_f32_16x16x32_f16 v[90:93], v[126:129], v[58:61], v[90:93]
	v_mfma_f32_16x16x32_f16 v[98:101], v[130:133], v[58:61], v[98:101]
	v_mfma_f32_16x16x32_f16 v[34:37], v[134:137], v[58:61], v[34:37]
	v_mfma_f32_16x16x32_f16 v[58:61], v[114:117], v[102:105], v[86:89]
	v_mfma_f32_16x16x32_f16 v[86:89], v[118:121], v[102:105], v[94:97]
	v_mfma_f32_16x16x32_f16 v[78:81], v[122:125], v[102:105], v[78:81]
	v_mfma_f32_16x16x32_f16 v[70:73], v[126:129], v[102:105], v[70:73]
	v_mfma_f32_16x16x32_f16 v[62:65], v[130:133], v[102:105], v[62:65]
	v_mfma_f32_16x16x32_f16 v[50:53], v[134:137], v[102:105], v[50:53]
	v_mfma_f32_16x16x32_f16 v[54:57], v[114:117], v[106:109], v[54:57]
	v_mfma_f32_16x16x32_f16 v[46:49], v[118:121], v[106:109], v[46:49]
	v_mfma_f32_16x16x32_f16 v[42:45], v[122:125], v[106:109], v[42:45]
	v_mfma_f32_16x16x32_f16 v[38:41], v[126:129], v[106:109], v[38:41]
	v_mfma_f32_16x16x32_f16 v[30:33], v[130:133], v[106:109], v[30:33]
	v_mfma_f32_16x16x32_f16 v[26:29], v[134:137], v[106:109], v[26:29]
	v_mfma_f32_16x16x32_f16 v[22:25], v[114:117], v[110:113], v[22:25]
	v_mfma_f32_16x16x32_f16 v[18:21], v[118:121], v[110:113], v[18:21]
	v_mfma_f32_16x16x32_f16 v[12:15], v[122:125], v[110:113], v[14:17]
	v_mfma_f32_16x16x32_f16 v[8:11], v[126:129], v[110:113], v[8:11]
	v_mfma_f32_16x16x32_f16 v[4:7], v[130:133], v[110:113], v[4:7]
	v_mfma_f32_16x16x32_f16 v[0:3], v[134:137], v[110:113], v[0:3]
	s_movk_i32 s0, 0x3400
	v_mad_u32_u24 v94, v144, s0, 0
	v_lshlrev_b32_e32 v16, 3, v145
	v_mul_u32_u24_e32 v17, 0xd0, v143
	v_add3_u32 v95, v94, v16, v17
	v_cvt_pk_f16_f32 v17, v68, v69
	v_cvt_pk_f16_f32 v16, v66, v67
	v_cvt_pk_f16_f32 v67, v76, v77
	v_cvt_pk_f16_f32 v66, v74, v75
	s_barrier
	ds_write2_b64 v95, v[16:17], v[66:67] offset1:4
	v_cvt_pk_f16_f32 v17, v84, v85
	v_cvt_pk_f16_f32 v16, v82, v83
	v_cvt_pk_f16_f32 v67, v92, v93
	v_cvt_pk_f16_f32 v66, v90, v91
	s_mov_b32 s0, 0x15555556
	ds_write2_b64 v95, v[16:17], v[66:67] offset0:8 offset1:12
	v_cvt_pk_f16_f32 v17, v100, v101
	v_cvt_pk_f16_f32 v16, v98, v99
	v_cvt_pk_f16_f32 v37, v36, v37
	v_cvt_pk_f16_f32 v36, v34, v35
	v_cvt_pk_f16_f32 v7, v6, v7
	v_cvt_pk_f16_f32 v6, v4, v5
	v_mul_hi_u32 v4, v140, s0
	ds_write2_b64 v95, v[16:17], v[36:37] offset0:16 offset1:20
	v_cvt_pk_f16_f32 v17, v60, v61
	v_cvt_pk_f16_f32 v16, v58, v59
	v_cvt_pk_f16_f32 v35, v88, v89
	v_cvt_pk_f16_f32 v34, v86, v87
	v_add_u32_e32 v36, 0x800, v95
	v_cvt_pk_f16_f32 v21, v20, v21
	v_cvt_pk_f16_f32 v20, v18, v19
	v_add_u32_e32 v18, 0x2000, v95
	v_cvt_pk_f16_f32 v15, v14, v15
	v_cvt_pk_f16_f32 v14, v12, v13
	v_cvt_pk_f16_f32 v11, v10, v11
	v_cvt_pk_f16_f32 v10, v8, v9
	v_cvt_pk_f16_f32 v3, v2, v3
	v_cvt_pk_f16_f32 v2, v0, v1
	v_mul_u32_u24_e32 v0, 12, v4
	ds_write2_b64 v36, v[16:17], v[34:35] offset0:160 offset1:164
	v_cvt_pk_f16_f32 v17, v80, v81
	v_cvt_pk_f16_f32 v16, v78, v79
	v_cvt_pk_f16_f32 v35, v72, v73
	v_cvt_pk_f16_f32 v34, v70, v71
	ds_write2_b64 v18, v[14:15], v[10:11] offset0:232 offset1:236
	v_add_u32_e32 v10, s13, v142
	v_sub_u32_e32 v5, v140, v0
	ds_write2_b64 v36, v[16:17], v[34:35] offset0:168 offset1:172
	v_cvt_pk_f16_f32 v17, v64, v65
	v_cvt_pk_f16_f32 v16, v62, v63
	v_cvt_pk_f16_f32 v35, v52, v53
	v_cvt_pk_f16_f32 v34, v50, v51
	v_lshl_add_u32 v12, v5, 3, v10
	ds_write2_b64 v36, v[16:17], v[34:35] offset0:176 offset1:180
	v_cvt_pk_f16_f32 v17, v56, v57
	v_cvt_pk_f16_f32 v16, v54, v55
	v_cvt_pk_f16_f32 v35, v48, v49
	v_cvt_pk_f16_f32 v34, v46, v47
	v_add_u32_e32 v36, 0x1800, v95
	v_lshrrev_b32_e32 v0, 10, v12
	v_mov_b32_e32 v1, 0
	ds_write2_b64 v36, v[16:17], v[34:35] offset0:64 offset1:68
	v_cvt_pk_f16_f32 v17, v44, v45
	v_cvt_pk_f16_f32 v16, v42, v43
	v_cvt_pk_f16_f32 v35, v40, v41
	v_cvt_pk_f16_f32 v34, v38, v39
	ds_write2_b64 v18, v[6:7], v[2:3] offset0:240 offset1:244
	v_add_u32_e32 v11, s12, v141
	v_lshlrev_b64 v[2:3], 23, v[0:1]
	ds_write2_b64 v36, v[16:17], v[34:35] offset0:72 offset1:76
	v_cvt_pk_f16_f32 v17, v32, v33
	v_cvt_pk_f16_f32 v16, v30, v31
	v_cvt_pk_f16_f32 v29, v28, v29
	v_cvt_pk_f16_f32 v28, v26, v27
	v_lshl_add_u64 v[6:7], s[8:9], 0, v[2:3]
	v_or_b32_e32 v2, v11, v4
	ds_write2_b64 v36, v[16:17], v[28:29] offset0:80 offset1:84
	v_cvt_pk_f16_f32 v17, v24, v25
	v_cvt_pk_f16_f32 v16, v22, v23
	v_ashrrev_i32_e32 v3, 31, v2
	ds_write2_b64 v18, v[16:17], v[20:21] offset0:224 offset1:228
	v_lshlrev_b64 v[8:9], 11, v[2:3]
	v_mul_u32_u24_e32 v0, 0xd0, v4
	v_lshlrev_b32_e32 v2, 4, v5
	s_waitcnt lgkmcnt(0)
	s_barrier
	v_readfirstlane_b32 s14, v142
	v_add_u32_e32 v26, s12, v141
	s_cmp_lg_u32 s14, 0
	s_cbranch_scc1 .Lg1ep_wc1
	v_lshrrev_b32_e32 v20, 4, v140
	v_and_b32_e32 v21, 15, v140
	v_lshlrev_b32_e32 v22, 4, v21
	v_add_u32_e32 v23, 0x3340, v22
	v_cmp_lt_u32_e32 vcc, 11, v21
	v_mul_u32_u24_e32 v24, 0xd0, v20
	s_nop 1
	v_cndmask_b32_e32 v22, v22, v23, vcc
	v_add3_u32 v24, v94, v24, v22
	v_lshl_add_u32 v25, v21, 3, s13
	v_add_u32_e32 v26, v26, v20
	s_mov_b64 s[2:3], 0x2000
	v_lshrrev_b32_e32 v30, 10, v25
	v_mov_b32_e32 v31, 0
	v_lshlrev_b64 v[30:31], 23, v[30:31]
	v_lshl_add_u64 v[28:29], s[8:9], 0, v[30:31]
	v_and_b32_e32 v30, 0x3ff, v25
	v_lshlrev_b32_e32 v30, 1, v30
	v_lshl_add_u32 v30, v26, 11, v30
	v_mov_b32_e32 v31, 0
	v_lshl_add_u64 v[28:29], v[28:29], 0, v[30:31]
	ds_read_b128 v[32:35], v24
	ds_read_b128 v[36:39], v24 offset:832
	ds_read_b128 v[40:43], v24 offset:1664
	ds_read_b128 v[44:47], v24 offset:2496
	s_waitcnt lgkmcnt(3)
	global_store_dwordx4 v[28:29], v[32:35], off sc1
	v_lshl_add_u64 v[28:29], v[28:29], 0, s[2:3]
	s_waitcnt lgkmcnt(2)
	global_store_dwordx4 v[28:29], v[36:39], off sc1
	v_lshl_add_u64 v[28:29], v[28:29], 0, s[2:3]
	s_waitcnt lgkmcnt(1)
	global_store_dwordx4 v[28:29], v[40:43], off sc1
	v_lshl_add_u64 v[28:29], v[28:29], 0, s[2:3]
	s_waitcnt lgkmcnt(0)
	global_store_dwordx4 v[28:29], v[44:47], off sc1
	v_lshl_add_u64 v[28:29], v[28:29], 0, s[2:3]
	ds_read_b128 v[48:51], v24 offset:3328
	ds_read_b128 v[52:55], v24 offset:4160
	ds_read_b128 v[56:59], v24 offset:4992
	ds_read_b128 v[60:63], v24 offset:5824
	s_waitcnt lgkmcnt(3)
	global_store_dwordx4 v[28:29], v[48:51], off sc1
	v_lshl_add_u64 v[28:29], v[28:29], 0, s[2:3]
	s_waitcnt lgkmcnt(2)
	global_store_dwordx4 v[28:29], v[52:55], off sc1
	v_lshl_add_u64 v[28:29], v[28:29], 0, s[2:3]
	s_waitcnt lgkmcnt(1)
	global_store_dwordx4 v[28:29], v[56:59], off sc1
	v_lshl_add_u64 v[28:29], v[28:29], 0, s[2:3]
	s_waitcnt lgkmcnt(0)
	global_store_dwordx4 v[28:29], v[60:63], off sc1
	v_lshl_add_u64 v[28:29], v[28:29], 0, s[2:3]
	ds_read_b128 v[32:35], v24 offset:6656
	ds_read_b128 v[36:39], v24 offset:7488
	ds_read_b128 v[40:43], v24 offset:8320
	ds_read_b128 v[44:47], v24 offset:9152
	s_waitcnt lgkmcnt(3)
	global_store_dwordx4 v[28:29], v[32:35], off sc1
	v_lshl_add_u64 v[28:29], v[28:29], 0, s[2:3]
	s_waitcnt lgkmcnt(2)
	global_store_dwordx4 v[28:29], v[36:39], off sc1
	v_lshl_add_u64 v[28:29], v[28:29], 0, s[2:3]
	s_waitcnt lgkmcnt(1)
	global_store_dwordx4 v[28:29], v[40:43], off sc1
	v_lshl_add_u64 v[28:29], v[28:29], 0, s[2:3]
	s_waitcnt lgkmcnt(0)
	global_store_dwordx4 v[28:29], v[44:47], off sc1
	v_lshl_add_u64 v[28:29], v[28:29], 0, s[2:3]
	ds_read_b128 v[48:51], v24 offset:9984
	ds_read_b128 v[52:55], v24 offset:10816
	ds_read_b128 v[56:59], v24 offset:11648
	ds_read_b128 v[60:63], v24 offset:12480
	s_waitcnt lgkmcnt(3)
	global_store_dwordx4 v[28:29], v[48:51], off sc1
	v_lshl_add_u64 v[28:29], v[28:29], 0, s[2:3]
	s_waitcnt lgkmcnt(2)
	global_store_dwordx4 v[28:29], v[52:55], off sc1
	v_lshl_add_u64 v[28:29], v[28:29], 0, s[2:3]
	s_waitcnt lgkmcnt(1)
	global_store_dwordx4 v[28:29], v[56:59], off sc1
	v_lshl_add_u64 v[28:29], v[28:29], 0, s[2:3]
	s_waitcnt lgkmcnt(0)
	global_store_dwordx4 v[28:29], v[60:63], off sc1
	v_lshl_add_u64 v[28:29], v[28:29], 0, s[2:3]
	s_endpgm
.Lg1ep_wc1:
	v_lshrrev_b32_e32 v20, 3, v140
	v_and_b32_e32 v21, 7, v140
	v_mul_u32_u24_e32 v24, 0xd0, v20
	v_lshl_add_u32 v22, v21, 4, v94
	v_add3_u32 v24, v22, v24, 64
	v_lshl_add_u32 v25, v21, 3, s13
	v_add_u32_e32 v25, 0x80, v25
	v_add_u32_e32 v26, v26, v20
	s_mov_b64 s[2:3], 0x4000
	v_lshrrev_b32_e32 v30, 10, v25
	v_mov_b32_e32 v31, 0
	v_lshlrev_b64 v[30:31], 23, v[30:31]
	v_lshl_add_u64 v[28:29], s[8:9], 0, v[30:31]
	v_and_b32_e32 v30, 0x3ff, v25
	v_lshlrev_b32_e32 v30, 1, v30
	v_lshl_add_u32 v30, v26, 11, v30
	v_mov_b32_e32 v31, 0
	v_lshl_add_u64 v[28:29], v[28:29], 0, v[30:31]
	ds_read_b128 v[32:35], v24
	ds_read_b128 v[36:39], v24 offset:1664
	ds_read_b128 v[40:43], v24 offset:3328
	ds_read_b128 v[44:47], v24 offset:4992
	s_waitcnt lgkmcnt(3)
	global_store_dwordx4 v[28:29], v[32:35], off sc1
	v_lshl_add_u64 v[28:29], v[28:29], 0, s[2:3]
	s_waitcnt lgkmcnt(2)
	global_store_dwordx4 v[28:29], v[36:39], off sc1
	v_lshl_add_u64 v[28:29], v[28:29], 0, s[2:3]
	s_waitcnt lgkmcnt(1)
	global_store_dwordx4 v[28:29], v[40:43], off sc1
	v_lshl_add_u64 v[28:29], v[28:29], 0, s[2:3]
	s_waitcnt lgkmcnt(0)
	global_store_dwordx4 v[28:29], v[44:47], off sc1
	v_lshl_add_u64 v[28:29], v[28:29], 0, s[2:3]
	ds_read_b128 v[48:51], v24 offset:6656
	ds_read_b128 v[52:55], v24 offset:8320
	ds_read_b128 v[56:59], v24 offset:9984
	ds_read_b128 v[60:63], v24 offset:11648
	s_waitcnt lgkmcnt(3)
	global_store_dwordx4 v[28:29], v[48:51], off sc1
	v_lshl_add_u64 v[28:29], v[28:29], 0, s[2:3]
	s_waitcnt lgkmcnt(2)
	global_store_dwordx4 v[28:29], v[52:55], off sc1
	v_lshl_add_u64 v[28:29], v[28:29], 0, s[2:3]
	s_waitcnt lgkmcnt(1)
	global_store_dwordx4 v[28:29], v[56:59], off sc1
	v_lshl_add_u64 v[28:29], v[28:29], 0, s[2:3]
	s_waitcnt lgkmcnt(0)
	global_store_dwordx4 v[28:29], v[60:63], off sc1
	v_lshl_add_u64 v[28:29], v[28:29], 0, s[2:3]
	s_endpgm
	s_nop 0
	s_nop 0
	s_nop 0
	s_nop 0
	s_nop 0
	s_nop 0
	s_nop 0
	s_nop 0
	s_nop 0
	s_nop 0
	s_nop 0
	s_nop 0
	s_nop 0
	s_nop 0
	s_nop 0
	s_nop 0
	s_nop 0
	s_nop 0
	s_nop 0
	s_nop 0
	s_nop 0
	s_endpgm
